# speedup vs baseline: 1.0043x; 1.0005x over previous
.LBB2_13:
	s_waitcnt vmcnt(0)
	v_pk_add_f32 v[10:11], v[10:11], v[2:3]
	s_nop 0
	v_mul_f32_e32 v55, 0x3e4ccccd, v10
	v_max_f32 v55, v10, v55
	v_mul_f32_e32 v10, 0x3e4ccccd, v11
	v_max_f32 v57, v11, v10
	v_pk_add_f32 v[10:11], v[12:13], v[4:5]
	v_cndmask_b32_e32 v56, v67, v55, vcc
	v_mul_f32_e32 v12, 0x3e4ccccd, v10
	v_mul_f32_e32 v13, 0x3e4ccccd, v11
	v_cndmask_b32_e32 v58, v67, v57, vcc
	v_max_f32 v10, v10, v12
	v_max_f32 v11, v11, v13
	s_nop 0
	v_cndmask_b32_e32 v12, v67, v10, vcc
	v_cndmask_b32_e32 v13, v67, v11, vcc
	s_nop 1
	v_max_f32_dpp v56, v56, v56 quad_perm:[1,0,3,2] row_mask:0xf bank_mask:0xf bound_ctrl:1
	v_max_f32_dpp v58, v58, v58 quad_perm:[1,0,3,2] row_mask:0xf bank_mask:0xf bound_ctrl:1
	v_max_f32_dpp v12, v12, v12 quad_perm:[1,0,3,2] row_mask:0xf bank_mask:0xf bound_ctrl:1
	v_max_f32_dpp v13, v13, v13 quad_perm:[1,0,3,2] row_mask:0xf bank_mask:0xf bound_ctrl:1
	v_max_f32_dpp v56, v56, v56 quad_perm:[2,3,0,1] row_mask:0xf bank_mask:0xf bound_ctrl:1
	v_max_f32_dpp v58, v58, v58 quad_perm:[2,3,0,1] row_mask:0xf bank_mask:0xf bound_ctrl:1
	v_max_f32_dpp v12, v12, v12 quad_perm:[2,3,0,1] row_mask:0xf bank_mask:0xf bound_ctrl:1
	v_max_f32_dpp v13, v13, v13 quad_perm:[2,3,0,1] row_mask:0xf bank_mask:0xf bound_ctrl:1
	v_max_f32_dpp v56, v56, v56 row_half_mirror row_mask:0xf bank_mask:0xf bound_ctrl:1
	v_max_f32_dpp v58, v58, v58 row_half_mirror row_mask:0xf bank_mask:0xf bound_ctrl:1
	v_max_f32_dpp v12, v12, v12 row_half_mirror row_mask:0xf bank_mask:0xf bound_ctrl:1
	v_max_f32_dpp v13, v13, v13 row_half_mirror row_mask:0xf bank_mask:0xf bound_ctrl:1
	v_max_f32_dpp v56, v56, v56 row_mirror row_mask:0xf bank_mask:0xf bound_ctrl:1
	v_max_f32_dpp v58, v58, v58 row_mirror row_mask:0xf bank_mask:0xf bound_ctrl:1
	v_max_f32_dpp v12, v12, v12 row_mirror row_mask:0xf bank_mask:0xf bound_ctrl:1
	v_max_f32_dpp v13, v13, v13 row_mirror row_mask:0xf bank_mask:0xf bound_ctrl:1
	s_nop 0
	s_nop 0
	v_max_f32 v110, v54, v56
	v_max_f32 v112, v15, v12
	v_max_f32 v111, v16, v58
	v_max_f32 v113, v14, v13
	s_nop 0
	v_sub_f32_e32 v54, v54, v110
	v_sub_f32_e32 v10, v10, v112
	v_exp_f32_e32 v114, v54
	v_sub_f32_e32 v54, v55, v110
	v_sub_f32_e32 v55, v57, v111
	v_exp_f32_e32 v12, v10
	v_sub_f32_e32 v10, v11, v113
	v_exp_f32_e32 v54, v54
	v_exp_f32_e32 v55, v55
	v_exp_f32_e32 v13, v10
	v_cndmask_b32_e32 v12, 0, v12, vcc
	v_cndmask_b32_e32 v10, 0, v54, vcc
	v_cndmask_b32_e32 v11, 0, v55, vcc
	v_cndmask_b32_e32 v13, 0, v13, vcc
	v_mov_b32_e32 v83, v12
	v_mov_b32_e32 v102, v11
	v_mov_b32_e32 v80, v13
	v_mov_b32_e32 v106, v10
	s_nop 1
	v_add_f32_dpp v106, v106, v106 quad_perm:[1,0,3,2] row_mask:0xf bank_mask:0xf bound_ctrl:1
	v_add_f32_dpp v102, v102, v102 quad_perm:[1,0,3,2] row_mask:0xf bank_mask:0xf bound_ctrl:1
	v_add_f32_dpp v83, v83, v83 quad_perm:[1,0,3,2] row_mask:0xf bank_mask:0xf bound_ctrl:1
	v_add_f32_dpp v80, v80, v80 quad_perm:[1,0,3,2] row_mask:0xf bank_mask:0xf bound_ctrl:1
	v_add_f32_dpp v106, v106, v106 quad_perm:[2,3,0,1] row_mask:0xf bank_mask:0xf bound_ctrl:1
	v_add_f32_dpp v102, v102, v102 quad_perm:[2,3,0,1] row_mask:0xf bank_mask:0xf bound_ctrl:1
	v_add_f32_dpp v83, v83, v83 quad_perm:[2,3,0,1] row_mask:0xf bank_mask:0xf bound_ctrl:1
	v_add_f32_dpp v80, v80, v80 quad_perm:[2,3,0,1] row_mask:0xf bank_mask:0xf bound_ctrl:1
	v_add_f32_dpp v106, v106, v106 row_half_mirror row_mask:0xf bank_mask:0xf bound_ctrl:1
	v_add_f32_dpp v102, v102, v102 row_half_mirror row_mask:0xf bank_mask:0xf bound_ctrl:1
	v_add_f32_dpp v83, v83, v83 row_half_mirror row_mask:0xf bank_mask:0xf bound_ctrl:1
	v_add_f32_dpp v80, v80, v80 row_half_mirror row_mask:0xf bank_mask:0xf bound_ctrl:1
	v_add_f32_dpp v106, v106, v106 row_mirror row_mask:0xf bank_mask:0xf bound_ctrl:1
	v_add_f32_dpp v102, v102, v102 row_mirror row_mask:0xf bank_mask:0xf bound_ctrl:1
	v_add_f32_dpp v83, v83, v83 row_mirror row_mask:0xf bank_mask:0xf bound_ctrl:1
	v_add_f32_dpp v80, v80, v80 row_mirror row_mask:0xf bank_mask:0xf bound_ctrl:1
	s_nop 0
	s_cmp_eq_u32 s24, 0
	s_cbranch_scc1 .LBB2_15
	v_cvt_f16_f32_e32 v54, v114
	v_pk_mul_f16 v109, v54, v109 op_sel_hi:[0,1]
	v_pk_mul_f16 v108, v54, v108 op_sel_hi:[0,1]
	v_pk_mul_f16 v107, v54, v107 op_sel_hi:[0,1]
	v_pk_mul_f16 v105, v54, v105 op_sel_hi:[0,1]
.LBB2_15:
	v_sub_f32_e32 v16, v16, v111
	v_exp_f32_e32 v115, v16
	s_cmp_eq_u32 s24, 0
	s_cbranch_scc1 .LBB2_17
	v_cvt_f16_f32_e32 v16, v115
	v_pk_mul_f16 v97, v16, v97 op_sel_hi:[0,1]
	v_pk_mul_f16 v95, v16, v95 op_sel_hi:[0,1]
	v_pk_mul_f16 v94, v16, v94 op_sel_hi:[0,1]
	v_pk_mul_f16 v92, v16, v92 op_sel_hi:[0,1]
.LBB2_17:
	v_sub_f32_e32 v15, v15, v112
	v_exp_f32_e32 v116, v15
	s_cmp_eq_u32 s24, 0
	s_cbranch_scc1 .LBB2_19
	v_cvt_f16_f32_e32 v15, v116
	v_pk_mul_f16 v90, v15, v90 op_sel_hi:[0,1]
	v_pk_mul_f16 v89, v15, v89 op_sel_hi:[0,1]
	v_pk_mul_f16 v88, v15, v88 op_sel_hi:[0,1]
	v_pk_mul_f16 v87, v15, v87 op_sel_hi:[0,1]
.LBB2_19:
	v_sub_f32_e32 v14, v14, v113
	v_exp_f32_e32 v117, v14
	s_cmp_eq_u32 s24, 0
	s_cbranch_scc1 .LBB2_21
	v_cvt_f16_f32_e32 v14, v117
	v_pk_mul_f16 v85, v14, v85 op_sel_hi:[0,1]
	v_pk_mul_f16 v84, v14, v84 op_sel_hi:[0,1]
	v_pk_mul_f16 v82, v14, v82 op_sel_hi:[0,1]
	v_pk_mul_f16 v81, v14, v81 op_sel_hi:[0,1]
